# speedup vs baseline: 1.0332x; 1.0065x over previous
_Z11prep_kernelPKfS0_S0_PDF16_PfPiS0_S1_:
	s_add_u32 s4, s2, 64
	s_sub_u32 s5, s2, 0xa1
	s_cmpk_lt_u32 s2, 0xa1
	s_cselect_b32 s2, s4, s5
	s_cmpk_lt_u32 s2, 0xc1
	s_mov_b64 s[4:5], -1
	s_cbranch_scc0 .LBB0_51
	s_cmpk_lg_i32 s2, 0xc0
	s_cbranch_scc0 .LBB0_11
	s_cmp_gt_u32 s2, 63
	s_cbranch_scc0 .LBB0_8
	s_load_dwordx4 s[4:7], s[0:1], 0x0
	s_load_dwordx2 s[28:29], s[0:1], 0x20
	s_sub_u32 s3, s2, 64
	v_readfirstlane_b32 s23, v0
	v_and_b32_e32 v1, 63, v0
	v_lshlrev_b32_e32 v100, 4, v1
	s_lshr_b32 s23, s23, 6
	s_lshr_b32 s27, s3, 1
	s_and_b32 s30, s3, 1
	s_lshl_b32 s8, s27, 12
	s_lshl_b32 s9, s23, 6
	s_add_u32 s8, s8, s9
	s_lshl_b32 s10, s23, 15
	s_lshl_b32 s9, s30, 10
	s_add_u32 s10, s10, s9
	s_waitcnt lgkmcnt(0)
	s_add_u32 s20, s4, s8
	s_addc_u32 s21, s5, 0
	s_add_u32 s24, s6, s10
	s_addc_u32 s25, s7, 0
	global_load_dwordx4 v[34:37], v100, s[24:25]
	global_load_dwordx4 v[38:41], v100, s[24:25] offset:2048
	s_add_u32 s24, s24, 0x1000
	s_addc_u32 s25, s25, 0
	s_load_dwordx8 s[32:39], s[20:21], 0x0
	s_load_dwordx8 s[40:47], s[20:21], 0x200
	s_load_dwordx8 s[48:55], s[20:21], 0x400
	s_load_dwordx8 s[56:63], s[20:21], 0x600
	s_load_dwordx8 s[64:71], s[20:21], 0x800
	s_load_dwordx8 s[72:79], s[20:21], 0xa00
	s_load_dwordx8 s[80:87], s[20:21], 0xc00
	s_load_dwordx8 s[88:95], s[20:21], 0xe00
	global_load_dwordx4 v[42:45], v100, s[24:25]
	global_load_dwordx4 v[46:49], v100, s[24:25] offset:2048
	s_add_u32 s24, s24, 0x1000
	s_addc_u32 s25, s25, 0
	global_load_dwordx4 v[50:53], v100, s[24:25]
	global_load_dwordx4 v[54:57], v100, s[24:25] offset:2048
	s_add_u32 s24, s24, 0x1000
	s_addc_u32 s25, s25, 0
	global_load_dwordx4 v[58:61], v100, s[24:25]
	global_load_dwordx4 v[62:65], v100, s[24:25] offset:2048
	s_add_u32 s24, s24, 0x1000
	s_addc_u32 s25, s25, 0
	global_load_dwordx4 v[66:69], v100, s[24:25]
	global_load_dwordx4 v[70:73], v100, s[24:25] offset:2048
	s_add_u32 s24, s24, 0x1000
	s_addc_u32 s25, s25, 0
	global_load_dwordx4 v[74:77], v100, s[24:25]
	global_load_dwordx4 v[78:81], v100, s[24:25] offset:2048
	s_add_u32 s24, s24, 0x1000
	s_addc_u32 s25, s25, 0
	global_load_dwordx4 v[82:85], v100, s[24:25]
	global_load_dwordx4 v[86:89], v100, s[24:25] offset:2048
	s_add_u32 s24, s24, 0x1000
	s_addc_u32 s25, s25, 0
	global_load_dwordx4 v[90:93], v100, s[24:25]
	global_load_dwordx4 v[94:97], v100, s[24:25] offset:2048
	v_mov_b64_e32 v[2:3], 0
	v_mov_b64_e32 v[4:5], 0
	v_mov_b64_e32 v[6:7], 0
	v_mov_b64_e32 v[8:9], 0
	v_mov_b64_e32 v[10:11], 0
	v_mov_b64_e32 v[12:13], 0
	v_mov_b64_e32 v[14:15], 0
	v_mov_b64_e32 v[16:17], 0
	v_mov_b64_e32 v[18:19], 0
	v_mov_b64_e32 v[20:21], 0
	v_mov_b64_e32 v[22:23], 0
	v_mov_b64_e32 v[24:25], 0
	v_mov_b64_e32 v[26:27], 0
	v_mov_b64_e32 v[28:29], 0
	v_mov_b64_e32 v[30:31], 0
	v_mov_b64_e32 v[32:33], 0
	s_waitcnt lgkmcnt(0)
	s_waitcnt vmcnt(15)
	v_pk_fma_f32 v[2:3], s[32:33], v[34:35], v[2:3] op_sel_hi:[0,1,1]
	v_pk_fma_f32 v[4:5], s[32:33], v[36:37], v[4:5] op_sel_hi:[0,1,1]
	v_pk_fma_f32 v[6:7], s[40:41], v[34:35], v[6:7] op_sel_hi:[0,1,1]
	v_pk_fma_f32 v[8:9], s[40:41], v[36:37], v[8:9] op_sel_hi:[0,1,1]
	v_pk_fma_f32 v[10:11], s[48:49], v[34:35], v[10:11] op_sel_hi:[0,1,1]
	v_pk_fma_f32 v[12:13], s[48:49], v[36:37], v[12:13] op_sel_hi:[0,1,1]
	v_pk_fma_f32 v[14:15], s[56:57], v[34:35], v[14:15] op_sel_hi:[0,1,1]
	v_pk_fma_f32 v[16:17], s[56:57], v[36:37], v[16:17] op_sel_hi:[0,1,1]
	v_pk_fma_f32 v[18:19], s[64:65], v[34:35], v[18:19] op_sel_hi:[0,1,1]
	v_pk_fma_f32 v[20:21], s[64:65], v[36:37], v[20:21] op_sel_hi:[0,1,1]
	v_pk_fma_f32 v[22:23], s[72:73], v[34:35], v[22:23] op_sel_hi:[0,1,1]
	v_pk_fma_f32 v[24:25], s[72:73], v[36:37], v[24:25] op_sel_hi:[0,1,1]
	v_pk_fma_f32 v[26:27], s[80:81], v[34:35], v[26:27] op_sel_hi:[0,1,1]
	v_pk_fma_f32 v[28:29], s[80:81], v[36:37], v[28:29] op_sel_hi:[0,1,1]
	v_pk_fma_f32 v[30:31], s[88:89], v[34:35], v[30:31] op_sel_hi:[0,1,1]
	v_pk_fma_f32 v[32:33], s[88:89], v[36:37], v[32:33] op_sel_hi:[0,1,1]
	s_waitcnt vmcnt(14)
	v_pk_fma_f32 v[2:3], s[32:33], v[38:39], v[2:3] op_sel:[1,0,0]
	v_pk_fma_f32 v[4:5], s[32:33], v[40:41], v[4:5] op_sel:[1,0,0]
	v_pk_fma_f32 v[6:7], s[40:41], v[38:39], v[6:7] op_sel:[1,0,0]
	v_pk_fma_f32 v[8:9], s[40:41], v[40:41], v[8:9] op_sel:[1,0,0]
	v_pk_fma_f32 v[10:11], s[48:49], v[38:39], v[10:11] op_sel:[1,0,0]
	v_pk_fma_f32 v[12:13], s[48:49], v[40:41], v[12:13] op_sel:[1,0,0]
	v_pk_fma_f32 v[14:15], s[56:57], v[38:39], v[14:15] op_sel:[1,0,0]
	v_pk_fma_f32 v[16:17], s[56:57], v[40:41], v[16:17] op_sel:[1,0,0]
	v_pk_fma_f32 v[18:19], s[64:65], v[38:39], v[18:19] op_sel:[1,0,0]
	v_pk_fma_f32 v[20:21], s[64:65], v[40:41], v[20:21] op_sel:[1,0,0]
	v_pk_fma_f32 v[22:23], s[72:73], v[38:39], v[22:23] op_sel:[1,0,0]
	v_pk_fma_f32 v[24:25], s[72:73], v[40:41], v[24:25] op_sel:[1,0,0]
	v_pk_fma_f32 v[26:27], s[80:81], v[38:39], v[26:27] op_sel:[1,0,0]
	v_pk_fma_f32 v[28:29], s[80:81], v[40:41], v[28:29] op_sel:[1,0,0]
	v_pk_fma_f32 v[30:31], s[88:89], v[38:39], v[30:31] op_sel:[1,0,0]
	v_pk_fma_f32 v[32:33], s[88:89], v[40:41], v[32:33] op_sel:[1,0,0]
	s_waitcnt vmcnt(13)
	v_pk_fma_f32 v[2:3], s[34:35], v[42:43], v[2:3] op_sel_hi:[0,1,1]
	v_pk_fma_f32 v[4:5], s[34:35], v[44:45], v[4:5] op_sel_hi:[0,1,1]
	v_pk_fma_f32 v[6:7], s[42:43], v[42:43], v[6:7] op_sel_hi:[0,1,1]
	v_pk_fma_f32 v[8:9], s[42:43], v[44:45], v[8:9] op_sel_hi:[0,1,1]
	v_pk_fma_f32 v[10:11], s[50:51], v[42:43], v[10:11] op_sel_hi:[0,1,1]
	v_pk_fma_f32 v[12:13], s[50:51], v[44:45], v[12:13] op_sel_hi:[0,1,1]
	v_pk_fma_f32 v[14:15], s[58:59], v[42:43], v[14:15] op_sel_hi:[0,1,1]
	v_pk_fma_f32 v[16:17], s[58:59], v[44:45], v[16:17] op_sel_hi:[0,1,1]
	v_pk_fma_f32 v[18:19], s[66:67], v[42:43], v[18:19] op_sel_hi:[0,1,1]
	v_pk_fma_f32 v[20:21], s[66:67], v[44:45], v[20:21] op_sel_hi:[0,1,1]
	v_pk_fma_f32 v[22:23], s[74:75], v[42:43], v[22:23] op_sel_hi:[0,1,1]
	v_pk_fma_f32 v[24:25], s[74:75], v[44:45], v[24:25] op_sel_hi:[0,1,1]
	v_pk_fma_f32 v[26:27], s[82:83], v[42:43], v[26:27] op_sel_hi:[0,1,1]
	v_pk_fma_f32 v[28:29], s[82:83], v[44:45], v[28:29] op_sel_hi:[0,1,1]
	v_pk_fma_f32 v[30:31], s[90:91], v[42:43], v[30:31] op_sel_hi:[0,1,1]
	v_pk_fma_f32 v[32:33], s[90:91], v[44:45], v[32:33] op_sel_hi:[0,1,1]
	s_waitcnt vmcnt(12)
	v_pk_fma_f32 v[2:3], s[34:35], v[46:47], v[2:3] op_sel:[1,0,0]
	v_pk_fma_f32 v[4:5], s[34:35], v[48:49], v[4:5] op_sel:[1,0,0]
	v_pk_fma_f32 v[6:7], s[42:43], v[46:47], v[6:7] op_sel:[1,0,0]
	v_pk_fma_f32 v[8:9], s[42:43], v[48:49], v[8:9] op_sel:[1,0,0]
	v_pk_fma_f32 v[10:11], s[50:51], v[46:47], v[10:11] op_sel:[1,0,0]
	v_pk_fma_f32 v[12:13], s[50:51], v[48:49], v[12:13] op_sel:[1,0,0]
	v_pk_fma_f32 v[14:15], s[58:59], v[46:47], v[14:15] op_sel:[1,0,0]
	v_pk_fma_f32 v[16:17], s[58:59], v[48:49], v[16:17] op_sel:[1,0,0]
	v_pk_fma_f32 v[18:19], s[66:67], v[46:47], v[18:19] op_sel:[1,0,0]
	v_pk_fma_f32 v[20:21], s[66:67], v[48:49], v[20:21] op_sel:[1,0,0]
	v_pk_fma_f32 v[22:23], s[74:75], v[46:47], v[22:23] op_sel:[1,0,0]
	v_pk_fma_f32 v[24:25], s[74:75], v[48:49], v[24:25] op_sel:[1,0,0]
	v_pk_fma_f32 v[26:27], s[82:83], v[46:47], v[26:27] op_sel:[1,0,0]
	v_pk_fma_f32 v[28:29], s[82:83], v[48:49], v[28:29] op_sel:[1,0,0]
	v_pk_fma_f32 v[30:31], s[90:91], v[46:47], v[30:31] op_sel:[1,0,0]
	v_pk_fma_f32 v[32:33], s[90:91], v[48:49], v[32:33] op_sel:[1,0,0]
	s_waitcnt vmcnt(11)
	v_pk_fma_f32 v[2:3], s[36:37], v[50:51], v[2:3] op_sel_hi:[0,1,1]
	v_pk_fma_f32 v[4:5], s[36:37], v[52:53], v[4:5] op_sel_hi:[0,1,1]
	v_pk_fma_f32 v[6:7], s[44:45], v[50:51], v[6:7] op_sel_hi:[0,1,1]
	v_pk_fma_f32 v[8:9], s[44:45], v[52:53], v[8:9] op_sel_hi:[0,1,1]
	v_pk_fma_f32 v[10:11], s[52:53], v[50:51], v[10:11] op_sel_hi:[0,1,1]
	v_pk_fma_f32 v[12:13], s[52:53], v[52:53], v[12:13] op_sel_hi:[0,1,1]
	v_pk_fma_f32 v[14:15], s[60:61], v[50:51], v[14:15] op_sel_hi:[0,1,1]
	v_pk_fma_f32 v[16:17], s[60:61], v[52:53], v[16:17] op_sel_hi:[0,1,1]
	v_pk_fma_f32 v[18:19], s[68:69], v[50:51], v[18:19] op_sel_hi:[0,1,1]
	v_pk_fma_f32 v[20:21], s[68:69], v[52:53], v[20:21] op_sel_hi:[0,1,1]
	v_pk_fma_f32 v[22:23], s[76:77], v[50:51], v[22:23] op_sel_hi:[0,1,1]
	v_pk_fma_f32 v[24:25], s[76:77], v[52:53], v[24:25] op_sel_hi:[0,1,1]
	v_pk_fma_f32 v[26:27], s[84:85], v[50:51], v[26:27] op_sel_hi:[0,1,1]
	v_pk_fma_f32 v[28:29], s[84:85], v[52:53], v[28:29] op_sel_hi:[0,1,1]
	v_pk_fma_f32 v[30:31], s[92:93], v[50:51], v[30:31] op_sel_hi:[0,1,1]
	v_pk_fma_f32 v[32:33], s[92:93], v[52:53], v[32:33] op_sel_hi:[0,1,1]
	s_waitcnt vmcnt(10)
	v_pk_fma_f32 v[2:3], s[36:37], v[54:55], v[2:3] op_sel:[1,0,0]
	v_pk_fma_f32 v[4:5], s[36:37], v[56:57], v[4:5] op_sel:[1,0,0]
	v_pk_fma_f32 v[6:7], s[44:45], v[54:55], v[6:7] op_sel:[1,0,0]
	v_pk_fma_f32 v[8:9], s[44:45], v[56:57], v[8:9] op_sel:[1,0,0]
	v_pk_fma_f32 v[10:11], s[52:53], v[54:55], v[10:11] op_sel:[1,0,0]
	v_pk_fma_f32 v[12:13], s[52:53], v[56:57], v[12:13] op_sel:[1,0,0]
	v_pk_fma_f32 v[14:15], s[60:61], v[54:55], v[14:15] op_sel:[1,0,0]
	v_pk_fma_f32 v[16:17], s[60:61], v[56:57], v[16:17] op_sel:[1,0,0]
	v_pk_fma_f32 v[18:19], s[68:69], v[54:55], v[18:19] op_sel:[1,0,0]
	v_pk_fma_f32 v[20:21], s[68:69], v[56:57], v[20:21] op_sel:[1,0,0]
	v_pk_fma_f32 v[22:23], s[76:77], v[54:55], v[22:23] op_sel:[1,0,0]
	v_pk_fma_f32 v[24:25], s[76:77], v[56:57], v[24:25] op_sel:[1,0,0]
	v_pk_fma_f32 v[26:27], s[84:85], v[54:55], v[26:27] op_sel:[1,0,0]
	v_pk_fma_f32 v[28:29], s[84:85], v[56:57], v[28:29] op_sel:[1,0,0]
	v_pk_fma_f32 v[30:31], s[92:93], v[54:55], v[30:31] op_sel:[1,0,0]
	v_pk_fma_f32 v[32:33], s[92:93], v[56:57], v[32:33] op_sel:[1,0,0]
	s_waitcnt vmcnt(9)
	v_pk_fma_f32 v[2:3], s[38:39], v[58:59], v[2:3] op_sel_hi:[0,1,1]
	v_pk_fma_f32 v[4:5], s[38:39], v[60:61], v[4:5] op_sel_hi:[0,1,1]
	v_pk_fma_f32 v[6:7], s[46:47], v[58:59], v[6:7] op_sel_hi:[0,1,1]
	v_pk_fma_f32 v[8:9], s[46:47], v[60:61], v[8:9] op_sel_hi:[0,1,1]
	v_pk_fma_f32 v[10:11], s[54:55], v[58:59], v[10:11] op_sel_hi:[0,1,1]
	v_pk_fma_f32 v[12:13], s[54:55], v[60:61], v[12:13] op_sel_hi:[0,1,1]
	v_pk_fma_f32 v[14:15], s[62:63], v[58:59], v[14:15] op_sel_hi:[0,1,1]
	v_pk_fma_f32 v[16:17], s[62:63], v[60:61], v[16:17] op_sel_hi:[0,1,1]
	v_pk_fma_f32 v[18:19], s[70:71], v[58:59], v[18:19] op_sel_hi:[0,1,1]
	v_pk_fma_f32 v[20:21], s[70:71], v[60:61], v[20:21] op_sel_hi:[0,1,1]
	v_pk_fma_f32 v[22:23], s[78:79], v[58:59], v[22:23] op_sel_hi:[0,1,1]
	v_pk_fma_f32 v[24:25], s[78:79], v[60:61], v[24:25] op_sel_hi:[0,1,1]
	v_pk_fma_f32 v[26:27], s[86:87], v[58:59], v[26:27] op_sel_hi:[0,1,1]
	v_pk_fma_f32 v[28:29], s[86:87], v[60:61], v[28:29] op_sel_hi:[0,1,1]
	v_pk_fma_f32 v[30:31], s[94:95], v[58:59], v[30:31] op_sel_hi:[0,1,1]
	v_pk_fma_f32 v[32:33], s[94:95], v[60:61], v[32:33] op_sel_hi:[0,1,1]
	s_waitcnt vmcnt(8)
	v_pk_fma_f32 v[2:3], s[38:39], v[62:63], v[2:3] op_sel:[1,0,0]
	v_pk_fma_f32 v[4:5], s[38:39], v[64:65], v[4:5] op_sel:[1,0,0]
	v_pk_fma_f32 v[6:7], s[46:47], v[62:63], v[6:7] op_sel:[1,0,0]
	v_pk_fma_f32 v[8:9], s[46:47], v[64:65], v[8:9] op_sel:[1,0,0]
	v_pk_fma_f32 v[10:11], s[54:55], v[62:63], v[10:11] op_sel:[1,0,0]
	v_pk_fma_f32 v[12:13], s[54:55], v[64:65], v[12:13] op_sel:[1,0,0]
	v_pk_fma_f32 v[14:15], s[62:63], v[62:63], v[14:15] op_sel:[1,0,0]
	v_pk_fma_f32 v[16:17], s[62:63], v[64:65], v[16:17] op_sel:[1,0,0]
	v_pk_fma_f32 v[18:19], s[70:71], v[62:63], v[18:19] op_sel:[1,0,0]
	v_pk_fma_f32 v[20:21], s[70:71], v[64:65], v[20:21] op_sel:[1,0,0]
	v_pk_fma_f32 v[22:23], s[78:79], v[62:63], v[22:23] op_sel:[1,0,0]
	v_pk_fma_f32 v[24:25], s[78:79], v[64:65], v[24:25] op_sel:[1,0,0]
	v_pk_fma_f32 v[26:27], s[86:87], v[62:63], v[26:27] op_sel:[1,0,0]
	v_pk_fma_f32 v[28:29], s[86:87], v[64:65], v[28:29] op_sel:[1,0,0]
	v_pk_fma_f32 v[30:31], s[94:95], v[62:63], v[30:31] op_sel:[1,0,0]
	v_pk_fma_f32 v[32:33], s[94:95], v[64:65], v[32:33] op_sel:[1,0,0]
	s_nop 0
	s_load_dwordx8 s[32:39], s[20:21], 0x20
	s_load_dwordx8 s[40:47], s[20:21], 0x220
	s_load_dwordx8 s[48:55], s[20:21], 0x420
	s_load_dwordx8 s[56:63], s[20:21], 0x620
	s_load_dwordx8 s[64:71], s[20:21], 0x820
	s_load_dwordx8 s[72:79], s[20:21], 0xa20
	s_load_dwordx8 s[80:87], s[20:21], 0xc20
	s_load_dwordx8 s[88:95], s[20:21], 0xe20
	s_waitcnt lgkmcnt(0)
	s_waitcnt vmcnt(7)
	v_pk_fma_f32 v[2:3], s[32:33], v[66:67], v[2:3] op_sel_hi:[0,1,1]
	v_pk_fma_f32 v[4:5], s[32:33], v[68:69], v[4:5] op_sel_hi:[0,1,1]
	v_pk_fma_f32 v[6:7], s[40:41], v[66:67], v[6:7] op_sel_hi:[0,1,1]
	v_pk_fma_f32 v[8:9], s[40:41], v[68:69], v[8:9] op_sel_hi:[0,1,1]
	v_pk_fma_f32 v[10:11], s[48:49], v[66:67], v[10:11] op_sel_hi:[0,1,1]
	v_pk_fma_f32 v[12:13], s[48:49], v[68:69], v[12:13] op_sel_hi:[0,1,1]
	v_pk_fma_f32 v[14:15], s[56:57], v[66:67], v[14:15] op_sel_hi:[0,1,1]
	v_pk_fma_f32 v[16:17], s[56:57], v[68:69], v[16:17] op_sel_hi:[0,1,1]
	v_pk_fma_f32 v[18:19], s[64:65], v[66:67], v[18:19] op_sel_hi:[0,1,1]
	v_pk_fma_f32 v[20:21], s[64:65], v[68:69], v[20:21] op_sel_hi:[0,1,1]
	v_pk_fma_f32 v[22:23], s[72:73], v[66:67], v[22:23] op_sel_hi:[0,1,1]
	v_pk_fma_f32 v[24:25], s[72:73], v[68:69], v[24:25] op_sel_hi:[0,1,1]
	v_pk_fma_f32 v[26:27], s[80:81], v[66:67], v[26:27] op_sel_hi:[0,1,1]
	v_pk_fma_f32 v[28:29], s[80:81], v[68:69], v[28:29] op_sel_hi:[0,1,1]
	v_pk_fma_f32 v[30:31], s[88:89], v[66:67], v[30:31] op_sel_hi:[0,1,1]
	v_pk_fma_f32 v[32:33], s[88:89], v[68:69], v[32:33] op_sel_hi:[0,1,1]
	s_waitcnt vmcnt(6)
	v_pk_fma_f32 v[2:3], s[32:33], v[70:71], v[2:3] op_sel:[1,0,0]
	v_pk_fma_f32 v[4:5], s[32:33], v[72:73], v[4:5] op_sel:[1,0,0]
	v_pk_fma_f32 v[6:7], s[40:41], v[70:71], v[6:7] op_sel:[1,0,0]
	v_pk_fma_f32 v[8:9], s[40:41], v[72:73], v[8:9] op_sel:[1,0,0]
	v_pk_fma_f32 v[10:11], s[48:49], v[70:71], v[10:11] op_sel:[1,0,0]
	v_pk_fma_f32 v[12:13], s[48:49], v[72:73], v[12:13] op_sel:[1,0,0]
	v_pk_fma_f32 v[14:15], s[56:57], v[70:71], v[14:15] op_sel:[1,0,0]
	v_pk_fma_f32 v[16:17], s[56:57], v[72:73], v[16:17] op_sel:[1,0,0]
	v_pk_fma_f32 v[18:19], s[64:65], v[70:71], v[18:19] op_sel:[1,0,0]
	v_pk_fma_f32 v[20:21], s[64:65], v[72:73], v[20:21] op_sel:[1,0,0]
	v_pk_fma_f32 v[22:23], s[72:73], v[70:71], v[22:23] op_sel:[1,0,0]
	v_pk_fma_f32 v[24:25], s[72:73], v[72:73], v[24:25] op_sel:[1,0,0]
	v_pk_fma_f32 v[26:27], s[80:81], v[70:71], v[26:27] op_sel:[1,0,0]
	v_pk_fma_f32 v[28:29], s[80:81], v[72:73], v[28:29] op_sel:[1,0,0]
	v_pk_fma_f32 v[30:31], s[88:89], v[70:71], v[30:31] op_sel:[1,0,0]
	v_pk_fma_f32 v[32:33], s[88:89], v[72:73], v[32:33] op_sel:[1,0,0]
	s_waitcnt vmcnt(5)
	v_pk_fma_f32 v[2:3], s[34:35], v[74:75], v[2:3] op_sel_hi:[0,1,1]
	v_pk_fma_f32 v[4:5], s[34:35], v[76:77], v[4:5] op_sel_hi:[0,1,1]
	v_pk_fma_f32 v[6:7], s[42:43], v[74:75], v[6:7] op_sel_hi:[0,1,1]
	v_pk_fma_f32 v[8:9], s[42:43], v[76:77], v[8:9] op_sel_hi:[0,1,1]
	v_pk_fma_f32 v[10:11], s[50:51], v[74:75], v[10:11] op_sel_hi:[0,1,1]
	v_pk_fma_f32 v[12:13], s[50:51], v[76:77], v[12:13] op_sel_hi:[0,1,1]
	v_pk_fma_f32 v[14:15], s[58:59], v[74:75], v[14:15] op_sel_hi:[0,1,1]
	v_pk_fma_f32 v[16:17], s[58:59], v[76:77], v[16:17] op_sel_hi:[0,1,1]
	v_pk_fma_f32 v[18:19], s[66:67], v[74:75], v[18:19] op_sel_hi:[0,1,1]
	v_pk_fma_f32 v[20:21], s[66:67], v[76:77], v[20:21] op_sel_hi:[0,1,1]
	v_pk_fma_f32 v[22:23], s[74:75], v[74:75], v[22:23] op_sel_hi:[0,1,1]
	v_pk_fma_f32 v[24:25], s[74:75], v[76:77], v[24:25] op_sel_hi:[0,1,1]
	v_pk_fma_f32 v[26:27], s[82:83], v[74:75], v[26:27] op_sel_hi:[0,1,1]
	v_pk_fma_f32 v[28:29], s[82:83], v[76:77], v[28:29] op_sel_hi:[0,1,1]
	v_pk_fma_f32 v[30:31], s[90:91], v[74:75], v[30:31] op_sel_hi:[0,1,1]
	v_pk_fma_f32 v[32:33], s[90:91], v[76:77], v[32:33] op_sel_hi:[0,1,1]
	s_waitcnt vmcnt(4)
	v_pk_fma_f32 v[2:3], s[34:35], v[78:79], v[2:3] op_sel:[1,0,0]
	v_pk_fma_f32 v[4:5], s[34:35], v[80:81], v[4:5] op_sel:[1,0,0]
	v_pk_fma_f32 v[6:7], s[42:43], v[78:79], v[6:7] op_sel:[1,0,0]
	v_pk_fma_f32 v[8:9], s[42:43], v[80:81], v[8:9] op_sel:[1,0,0]
	v_pk_fma_f32 v[10:11], s[50:51], v[78:79], v[10:11] op_sel:[1,0,0]
	v_pk_fma_f32 v[12:13], s[50:51], v[80:81], v[12:13] op_sel:[1,0,0]
	v_pk_fma_f32 v[14:15], s[58:59], v[78:79], v[14:15] op_sel:[1,0,0]
	v_pk_fma_f32 v[16:17], s[58:59], v[80:81], v[16:17] op_sel:[1,0,0]
	v_pk_fma_f32 v[18:19], s[66:67], v[78:79], v[18:19] op_sel:[1,0,0]
	v_pk_fma_f32 v[20:21], s[66:67], v[80:81], v[20:21] op_sel:[1,0,0]
	v_pk_fma_f32 v[22:23], s[74:75], v[78:79], v[22:23] op_sel:[1,0,0]
	v_pk_fma_f32 v[24:25], s[74:75], v[80:81], v[24:25] op_sel:[1,0,0]
	v_pk_fma_f32 v[26:27], s[82:83], v[78:79], v[26:27] op_sel:[1,0,0]
	v_pk_fma_f32 v[28:29], s[82:83], v[80:81], v[28:29] op_sel:[1,0,0]
	v_pk_fma_f32 v[30:31], s[90:91], v[78:79], v[30:31] op_sel:[1,0,0]
	v_pk_fma_f32 v[32:33], s[90:91], v[80:81], v[32:33] op_sel:[1,0,0]
	s_waitcnt vmcnt(3)
	v_pk_fma_f32 v[2:3], s[36:37], v[82:83], v[2:3] op_sel_hi:[0,1,1]
	v_pk_fma_f32 v[4:5], s[36:37], v[84:85], v[4:5] op_sel_hi:[0,1,1]
	v_pk_fma_f32 v[6:7], s[44:45], v[82:83], v[6:7] op_sel_hi:[0,1,1]
	v_pk_fma_f32 v[8:9], s[44:45], v[84:85], v[8:9] op_sel_hi:[0,1,1]
	v_pk_fma_f32 v[10:11], s[52:53], v[82:83], v[10:11] op_sel_hi:[0,1,1]
	v_pk_fma_f32 v[12:13], s[52:53], v[84:85], v[12:13] op_sel_hi:[0,1,1]
	v_pk_fma_f32 v[14:15], s[60:61], v[82:83], v[14:15] op_sel_hi:[0,1,1]
	v_pk_fma_f32 v[16:17], s[60:61], v[84:85], v[16:17] op_sel_hi:[0,1,1]
	v_pk_fma_f32 v[18:19], s[68:69], v[82:83], v[18:19] op_sel_hi:[0,1,1]
	v_pk_fma_f32 v[20:21], s[68:69], v[84:85], v[20:21] op_sel_hi:[0,1,1]
	v_pk_fma_f32 v[22:23], s[76:77], v[82:83], v[22:23] op_sel_hi:[0,1,1]
	v_pk_fma_f32 v[24:25], s[76:77], v[84:85], v[24:25] op_sel_hi:[0,1,1]
	v_pk_fma_f32 v[26:27], s[84:85], v[82:83], v[26:27] op_sel_hi:[0,1,1]
	v_pk_fma_f32 v[28:29], s[84:85], v[84:85], v[28:29] op_sel_hi:[0,1,1]
	v_pk_fma_f32 v[30:31], s[92:93], v[82:83], v[30:31] op_sel_hi:[0,1,1]
	v_pk_fma_f32 v[32:33], s[92:93], v[84:85], v[32:33] op_sel_hi:[0,1,1]
	s_waitcnt vmcnt(2)
	v_pk_fma_f32 v[2:3], s[36:37], v[86:87], v[2:3] op_sel:[1,0,0]
	v_pk_fma_f32 v[4:5], s[36:37], v[88:89], v[4:5] op_sel:[1,0,0]
	v_pk_fma_f32 v[6:7], s[44:45], v[86:87], v[6:7] op_sel:[1,0,0]
	v_pk_fma_f32 v[8:9], s[44:45], v[88:89], v[8:9] op_sel:[1,0,0]
	v_pk_fma_f32 v[10:11], s[52:53], v[86:87], v[10:11] op_sel:[1,0,0]
	v_pk_fma_f32 v[12:13], s[52:53], v[88:89], v[12:13] op_sel:[1,0,0]
	v_pk_fma_f32 v[14:15], s[60:61], v[86:87], v[14:15] op_sel:[1,0,0]
	v_pk_fma_f32 v[16:17], s[60:61], v[88:89], v[16:17] op_sel:[1,0,0]
	v_pk_fma_f32 v[18:19], s[68:69], v[86:87], v[18:19] op_sel:[1,0,0]
	v_pk_fma_f32 v[20:21], s[68:69], v[88:89], v[20:21] op_sel:[1,0,0]
	v_pk_fma_f32 v[22:23], s[76:77], v[86:87], v[22:23] op_sel:[1,0,0]
	v_pk_fma_f32 v[24:25], s[76:77], v[88:89], v[24:25] op_sel:[1,0,0]
	v_pk_fma_f32 v[26:27], s[84:85], v[86:87], v[26:27] op_sel:[1,0,0]
	v_pk_fma_f32 v[28:29], s[84:85], v[88:89], v[28:29] op_sel:[1,0,0]
	v_pk_fma_f32 v[30:31], s[92:93], v[86:87], v[30:31] op_sel:[1,0,0]
	v_pk_fma_f32 v[32:33], s[92:93], v[88:89], v[32:33] op_sel:[1,0,0]
	s_waitcnt vmcnt(1)
	v_pk_fma_f32 v[2:3], s[38:39], v[90:91], v[2:3] op_sel_hi:[0,1,1]
	v_pk_fma_f32 v[4:5], s[38:39], v[92:93], v[4:5] op_sel_hi:[0,1,1]
	v_pk_fma_f32 v[6:7], s[46:47], v[90:91], v[6:7] op_sel_hi:[0,1,1]
	v_pk_fma_f32 v[8:9], s[46:47], v[92:93], v[8:9] op_sel_hi:[0,1,1]
	v_pk_fma_f32 v[10:11], s[54:55], v[90:91], v[10:11] op_sel_hi:[0,1,1]
	v_pk_fma_f32 v[12:13], s[54:55], v[92:93], v[12:13] op_sel_hi:[0,1,1]
	v_pk_fma_f32 v[14:15], s[62:63], v[90:91], v[14:15] op_sel_hi:[0,1,1]
	v_pk_fma_f32 v[16:17], s[62:63], v[92:93], v[16:17] op_sel_hi:[0,1,1]
	v_pk_fma_f32 v[18:19], s[70:71], v[90:91], v[18:19] op_sel_hi:[0,1,1]
	v_pk_fma_f32 v[20:21], s[70:71], v[92:93], v[20:21] op_sel_hi:[0,1,1]
	v_pk_fma_f32 v[22:23], s[78:79], v[90:91], v[22:23] op_sel_hi:[0,1,1]
	v_pk_fma_f32 v[24:25], s[78:79], v[92:93], v[24:25] op_sel_hi:[0,1,1]
	v_pk_fma_f32 v[26:27], s[86:87], v[90:91], v[26:27] op_sel_hi:[0,1,1]
	v_pk_fma_f32 v[28:29], s[86:87], v[92:93], v[28:29] op_sel_hi:[0,1,1]
	v_pk_fma_f32 v[30:31], s[94:95], v[90:91], v[30:31] op_sel_hi:[0,1,1]
	v_pk_fma_f32 v[32:33], s[94:95], v[92:93], v[32:33] op_sel_hi:[0,1,1]
	s_waitcnt vmcnt(0)
	v_pk_fma_f32 v[2:3], s[38:39], v[94:95], v[2:3] op_sel:[1,0,0]
	v_pk_fma_f32 v[4:5], s[38:39], v[96:97], v[4:5] op_sel:[1,0,0]
	v_pk_fma_f32 v[6:7], s[46:47], v[94:95], v[6:7] op_sel:[1,0,0]
	v_pk_fma_f32 v[8:9], s[46:47], v[96:97], v[8:9] op_sel:[1,0,0]
	v_pk_fma_f32 v[10:11], s[54:55], v[94:95], v[10:11] op_sel:[1,0,0]
	v_pk_fma_f32 v[12:13], s[54:55], v[96:97], v[12:13] op_sel:[1,0,0]
	v_pk_fma_f32 v[14:15], s[62:63], v[94:95], v[14:15] op_sel:[1,0,0]
	v_pk_fma_f32 v[16:17], s[62:63], v[96:97], v[16:17] op_sel:[1,0,0]
	v_pk_fma_f32 v[18:19], s[70:71], v[94:95], v[18:19] op_sel:[1,0,0]
	v_pk_fma_f32 v[20:21], s[70:71], v[96:97], v[20:21] op_sel:[1,0,0]
	v_pk_fma_f32 v[22:23], s[78:79], v[94:95], v[22:23] op_sel:[1,0,0]
	v_pk_fma_f32 v[24:25], s[78:79], v[96:97], v[24:25] op_sel:[1,0,0]
	v_pk_fma_f32 v[26:27], s[86:87], v[94:95], v[26:27] op_sel:[1,0,0]
	v_pk_fma_f32 v[28:29], s[86:87], v[96:97], v[28:29] op_sel:[1,0,0]
	v_pk_fma_f32 v[30:31], s[94:95], v[94:95], v[30:31] op_sel:[1,0,0]
	v_pk_fma_f32 v[32:33], s[94:95], v[96:97], v[32:33] op_sel:[1,0,0]
	s_lshl_b32 s9, s23, 13
	v_add_u32_e32 v98, s9, v100
	ds_write_b128 v98, v[2:5] offset:0
	ds_write_b128 v98, v[6:9] offset:1024
	ds_write_b128 v98, v[10:13] offset:2048
	ds_write_b128 v98, v[14:17] offset:3072
	ds_write_b128 v98, v[18:21] offset:4096
	ds_write_b128 v98, v[22:25] offset:5120
	ds_write_b128 v98, v[26:29] offset:6144
	ds_write_b128 v98, v[30:33] offset:7168
	s_lshl_b32 s9, s23, 10
	v_add_u32_e32 v99, s9, v100
	s_waitcnt lgkmcnt(0)
	s_barrier
	ds_read_b128 v[34:37], v99 offset:0
	ds_read_b128 v[38:41], v99 offset:8192
	ds_read_b128 v[42:45], v99 offset:16384
	ds_read_b128 v[46:49], v99 offset:24576
	ds_read_b128 v[50:53], v99 offset:32768
	ds_read_b128 v[54:57], v99 offset:40960
	ds_read_b128 v[58:61], v99 offset:49152
	ds_read_b128 v[62:65], v99 offset:57344
	s_lshl_b32 s8, s27, 3
	s_add_u32 s8, s8, s23
	s_lshl_b32 s8, s8, 11
	s_lshl_b32 s9, s30, 10
	s_add_u32 s8, s8, s9
	s_add_u32 s28, s28, s8
	s_addc_u32 s29, s29, 0
	s_waitcnt lgkmcnt(6)
	v_pk_add_f32 v[34:35], v[34:35], v[38:39]
	v_pk_add_f32 v[36:37], v[36:37], v[40:41]
	s_waitcnt lgkmcnt(5)
	v_pk_add_f32 v[34:35], v[34:35], v[42:43]
	v_pk_add_f32 v[36:37], v[36:37], v[44:45]
	s_waitcnt lgkmcnt(4)
	v_pk_add_f32 v[34:35], v[34:35], v[46:47]
	v_pk_add_f32 v[36:37], v[36:37], v[48:49]
	s_waitcnt lgkmcnt(3)
	v_pk_add_f32 v[34:35], v[34:35], v[50:51]
	v_pk_add_f32 v[36:37], v[36:37], v[52:53]
	s_waitcnt lgkmcnt(2)
	v_pk_add_f32 v[34:35], v[34:35], v[54:55]
	v_pk_add_f32 v[36:37], v[36:37], v[56:57]
	s_waitcnt lgkmcnt(1)
	v_pk_add_f32 v[34:35], v[34:35], v[58:59]
	v_pk_add_f32 v[36:37], v[36:37], v[60:61]
	s_waitcnt lgkmcnt(0)
	v_pk_add_f32 v[34:35], v[34:35], v[62:63]
	v_pk_add_f32 v[36:37], v[36:37], v[64:65]
	global_store_dwordx4 v100, v[34:37], s[28:29]
